# K3 writes the CSR edge array with nt stores (on top of plain edge staging loads in the hops)
# speedup vs baseline: 1.1304x; 1.0074x over previous
.LBB2_128:
	ds_read_b64 v[6:7], v2
	v_add_u32_e32 v0, 0x200, v0
	v_cmp_le_i32_e32 vcc, s4, v0
	v_add_u32_e32 v2, 0x1000, v2
	s_or_b64 s[0:1], vcc, s[0:1]
	s_waitcnt lgkmcnt(0)
	global_store_dwordx2 v[4:5], v[6:7], off nt
	v_lshl_add_u64 v[4:5], v[4:5], 0, s[2:3]
	s_andn2_b64 exec, exec, s[0:1]
	s_cbranch_execnz .LBB2_128
